# baseline (speedup 1.0000x reference)
.LBB0_35:
	s_or_b64 exec, exec, s[0:1]
	s_waitcnt vmcnt(14)
	v_mul_u32_u24_e32 v105, 0x880, v227
	s_waitcnt vmcnt(11)
	v_cvt_pk_f16_f32 v3, v150, v151
	v_cvt_pk_f16_f32 v2, v148, v149
	v_lshl_add_u32 v4, v1, 1, v105
	s_waitcnt vmcnt(10)
	v_cvt_pk_f16_f32 v1, v154, v155
	s_waitcnt lgkmcnt(0)
	v_cvt_pk_f16_f32 v0, v152, v153
	s_barrier
	v_lshl_or_b32 v233, v225, 6, v220
	v_mul_u32_u24_e32 v233, 0x110, v233
	v_add_u32_e32 v233, v233, v223
	v_add_u32_e32 v233, 0x10000, v233
	ds_read_b128 v[180:183], v233
	ds_read_b128 v[184:187], v233 offset:32
	ds_read_b128 v[188:191], v233 offset:64
	ds_read_b128 v[192:195], v233 offset:96
	ds_read_b128 v[196:199], v233 offset:128
	ds_read_b128 v[200:203], v233 offset:160
	ds_read_b128 v[204:207], v233 offset:192
	ds_read_b128 v[208:211], v233 offset:224
	ds_write2_b64 v4, v[2:3], v[0:1] offset1:34
	s_sleep 16
	s_waitcnt vmcnt(9)
	v_cvt_pk_f16_f32 v1, v166, v167
	v_cvt_pk_f16_f32 v0, v164, v165
	s_waitcnt vmcnt(8)
	v_cvt_pk_f16_f32 v3, v158, v159
	v_cvt_pk_f16_f32 v2, v156, v157
	ds_write2_b64 v4, v[0:1], v[2:3] offset0:68 offset1:102
	s_waitcnt vmcnt(7)
	v_cvt_pk_f16_f32 v1, v162, v163
	v_cvt_pk_f16_f32 v0, v160, v161
	s_waitcnt vmcnt(6)
	v_cvt_pk_f16_f32 v3, v170, v171
	v_cvt_pk_f16_f32 v2, v168, v169
	ds_write2_b64 v4, v[0:1], v[2:3] offset0:136 offset1:170
	s_waitcnt vmcnt(5)
	v_cvt_pk_f16_f32 v1, v174, v175
	v_cvt_pk_f16_f32 v0, v172, v173
	s_waitcnt vmcnt(4)
	v_cvt_pk_f16_f32 v3, v178, v179
	v_cvt_pk_f16_f32 v2, v176, v177
	ds_write2_b64 v4, v[0:1], v[2:3] offset0:204 offset1:238
	ds_read_b128 v[148:151], v233 offset:8704
	ds_read_b128 v[152:155], v233 offset:8736
	ds_read_b128 v[156:159], v233 offset:8768
	ds_read_b128 v[160:163], v233 offset:8800
	ds_read_b128 v[164:167], v233 offset:8832
	ds_read_b128 v[168:171], v233 offset:8864
	ds_read_b128 v[172:175], v233 offset:8896
	ds_read_b128 v[176:179], v233 offset:8928
	v_lshlrev_b32_e32 v2, 1, v228
	s_waitcnt vmcnt(1)
	v_cvt_pk_f16_f32 v1, v40, v41
	v_cvt_pk_f16_f32 v0, v38, v39
	v_mad_u32_u24 v3, v227, s6, v2
	ds_write_b64 v3, v[0:1] offset:34816
	s_waitcnt vmcnt(0)
	v_cvt_pk_f16_f32 v1, v36, v37
	v_cvt_pk_f16_f32 v0, v34, v35
	v_mad_u32_u24 v2, v229, s6, v2
	ds_write_b64 v2, v[0:1] offset:34816
	v_mov_b32_e32 v97, 0
	v_mov_b32_e32 v0, 0
	v_mov_b32_e32 v4, 0
	v_mov_b32_e32 v96, 0
	s_and_saveexec_b64 s[0:1], vcc
	s_cbranch_execz .LBB0_37
	v_lshl_add_u32 v1, v220, 1, v230
	v_or_b32_e32 v2, 0x21000, v1
	v_add_u32_e32 v1, 0x21040, v1
	ds_read_u16 v1, v1
	ds_read_u16 v2, v2
	v_cvt_f16_f32_e32 v0, v104
	s_waitcnt lgkmcnt(1)
	v_and_b32_e32 v4, 0xffff, v1
	v_pack_b32_f16 v0, v0, 0
	s_waitcnt lgkmcnt(0)
	v_and_b32_e32 v96, 0xffff, v2
